# MLA layer-0 peeled last key tile: QK^T with 8 K fragments in flight instead of 12 serial LDS round trips
# speedup vs baseline: 1.0015x; 1.0015x over previous
.LBB0_1042:
	v_add_u32_e32 v2, v230, v154
	ds_read_b128 v[4:7], v2 offset:44032
	ds_read_b128 v[8:11], v2 offset:44064
	ds_read_b128 v[12:15], v2 offset:44096
	ds_read_b128 v[238:241], v2 offset:44128
	ds_read_b128 v[146:149], v2 offset:44160
	ds_read_b128 v[150:153], v2 offset:44192
	ds_read_b128 v[248:251], v2 offset:44224
	ds_read_b128 v[252:255], v2 offset:44256
	s_waitcnt lgkmcnt(7)
	v_mfma_f32_32x32x16_bf16 v[82:97], v[4:7], v[142:145], 0
	ds_read_b128 v[4:7], v2 offset:44288
	s_waitcnt lgkmcnt(7)
	v_mfma_f32_32x32x16_bf16 v[82:97], v[8:11], v[138:141], v[82:97]
	ds_read_b128 v[8:11], v2 offset:44320
	s_waitcnt lgkmcnt(7)
	v_mfma_f32_32x32x16_bf16 v[82:97], v[12:15], v[134:137], v[82:97]
	ds_read_b128 v[12:15], v2 offset:44352
	s_waitcnt lgkmcnt(7)
	v_mfma_f32_32x32x16_bf16 v[82:97], v[238:241], v[130:133], v[82:97]
	ds_read_b128 v[238:241], v2 offset:44384
	v_max_f32_e32 v2, v236, v236
	s_waitcnt lgkmcnt(7)
	v_mfma_f32_32x32x16_bf16 v[82:97], v[146:149], v[126:129], v[82:97]
	s_waitcnt lgkmcnt(6)
	v_mfma_f32_32x32x16_bf16 v[82:97], v[150:153], v[122:125], v[82:97]
	s_waitcnt lgkmcnt(5)
	v_mfma_f32_32x32x16_bf16 v[82:97], v[248:251], v[118:121], v[82:97]
	s_waitcnt lgkmcnt(4)
	v_mfma_f32_32x32x16_bf16 v[82:97], v[252:255], v[114:117], v[82:97]
	s_waitcnt lgkmcnt(3)
	v_mfma_f32_32x32x16_bf16 v[82:97], v[4:7], v[110:113], v[82:97]
	s_waitcnt lgkmcnt(2)
	v_mfma_f32_32x32x16_bf16 v[82:97], v[8:11], v[106:109], v[82:97]
	s_waitcnt lgkmcnt(1)
	v_mfma_f32_32x32x16_bf16 v[82:97], v[12:15], v[102:105], v[82:97]
	s_waitcnt lgkmcnt(0)
	v_mfma_f32_32x32x16_bf16 v[82:97], v[238:241], v[98:101], v[82:97]
	s_nop 11
	v_max3_f32 v4, v82, s19, v83
	v_max3_f32 v4, v4, v84, v85
	v_max3_f32 v4, v4, v86, v87
	v_max3_f32 v4, v4, v88, v89
	v_max3_f32 v4, v4, v90, v91
	v_max3_f32 v4, v4, v92, v93
	v_max3_f32 v4, v4, v94, v95
	v_max3_f32 v4, v4, v96, v97
	v_mov_b32_e32 v5, v4
	s_nop 1
	v_permlane32_swap_b32_e32 v4, v5
	v_mul_f32_e32 v4, 0x3dd53b95, v4
	v_max_f32_e32 v4, v2, v4
	v_fma_f32 v5, v82, s20, -v4
	v_fma_f32 v6, v83, s20, -v4
	v_fma_f32 v7, v84, s20, -v4
	v_exp_f32_e32 v84, v5
	v_fma_f32 v9, v86, s20, -v4
	v_exp_f32_e32 v86, v6
	v_fma_f32 v8, v85, s20, -v4
	v_exp_f32_e32 v82, v7
	v_exp_f32_e32 v85, v8
	v_fma_f32 v10, v87, s20, -v4
	v_exp_f32_e32 v15, v9
	v_add_f32_e32 v6, 0, v84
	v_fma_f32 v11, v88, s20, -v4
	v_exp_f32_e32 v83, v10
	v_add_f32_e32 v6, v86, v6
	v_fma_f32 v12, v89, s20, -v4
	v_exp_f32_e32 v14, v11
	v_add_f32_e32 v6, v82, v6
	v_fma_f32 v13, v90, s20, -v4
	v_exp_f32_e32 v17, v12
	v_add_f32_e32 v6, v85, v6
	v_fma_f32 v87, v91, s20, -v4
	v_exp_f32_e32 v9, v13
	v_add_f32_e32 v6, v15, v6
	v_fma_f32 v88, v92, s20, -v4
	v_exp_f32_e32 v12, v87
	v_add_f32_e32 v6, v83, v6
	v_fma_f32 v89, v93, s20, -v4
	v_exp_f32_e32 v7, v88
	v_add_f32_e32 v6, v14, v6
	v_fma_f32 v90, v94, s20, -v4
	v_exp_f32_e32 v10, v89
	v_add_f32_e32 v6, v17, v6
	v_fma_f32 v91, v95, s20, -v4
	v_exp_f32_e32 v5, v90
	v_add_f32_e32 v6, v9, v6
	v_fma_f32 v92, v96, s20, -v4
	v_exp_f32_e32 v8, v91
	v_add_f32_e32 v6, v12, v6
	v_fma_f32 v93, v97, s20, -v4
	v_exp_f32_e32 v11, v92
	v_add_f32_e32 v6, v7, v6
	v_exp_f32_e32 v13, v93
	v_add_f32_e32 v6, v10, v6
	v_sub_f32_e32 v2, v236, v4
	v_add_f32_e32 v6, v5, v6
	v_exp_f32_e32 v2, v2
	v_add_f32_e32 v6, v8, v6
	v_add_f32_e32 v6, v11, v6
	v_add_f32_e32 v6, v13, v6
	v_mov_b32_e32 v87, v6
	v_cmp_neq_f32_e32 vcc, 1.0, v2
	s_nop 0
	v_permlane32_swap_b32_e32 v6, v87
	s_cbranch_vccz .LBB0_1044
	v_pk_mul_f32 v[80:81], v[80:81], v[2:3] op_sel_hi:[1,0]
	v_pk_mul_f32 v[78:79], v[78:79], v[2:3] op_sel_hi:[1,0]
	v_pk_mul_f32 v[76:77], v[76:77], v[2:3] op_sel_hi:[1,0]
	v_pk_mul_f32 v[74:75], v[74:75], v[2:3] op_sel_hi:[1,0]
	v_pk_mul_f32 v[72:73], v[72:73], v[2:3] op_sel_hi:[1,0]
	v_pk_mul_f32 v[70:71], v[70:71], v[2:3] op_sel_hi:[1,0]
	v_pk_mul_f32 v[68:69], v[68:69], v[2:3] op_sel_hi:[1,0]
	v_pk_mul_f32 v[66:67], v[66:67], v[2:3] op_sel_hi:[1,0]
	v_pk_mul_f32 v[64:65], v[64:65], v[2:3] op_sel_hi:[1,0]
	v_pk_mul_f32 v[62:63], v[62:63], v[2:3] op_sel_hi:[1,0]
	v_pk_mul_f32 v[60:61], v[60:61], v[2:3] op_sel_hi:[1,0]
	v_pk_mul_f32 v[58:59], v[58:59], v[2:3] op_sel_hi:[1,0]
	v_pk_mul_f32 v[56:57], v[56:57], v[2:3] op_sel_hi:[1,0]
	v_pk_mul_f32 v[54:55], v[54:55], v[2:3] op_sel_hi:[1,0]
	v_pk_mul_f32 v[52:53], v[52:53], v[2:3] op_sel_hi:[1,0]
	v_pk_mul_f32 v[50:51], v[50:51], v[2:3] op_sel_hi:[1,0]
	v_pk_mul_f32 v[48:49], v[48:49], v[2:3] op_sel_hi:[1,0]
	v_pk_mul_f32 v[46:47], v[46:47], v[2:3] op_sel_hi:[1,0]
	v_pk_mul_f32 v[44:45], v[44:45], v[2:3] op_sel_hi:[1,0]
	v_pk_mul_f32 v[42:43], v[42:43], v[2:3] op_sel_hi:[1,0]
	v_pk_mul_f32 v[40:41], v[40:41], v[2:3] op_sel_hi:[1,0]
	v_pk_mul_f32 v[38:39], v[38:39], v[2:3] op_sel_hi:[1,0]
	v_pk_mul_f32 v[36:37], v[36:37], v[2:3] op_sel_hi:[1,0]
	v_pk_mul_f32 v[34:35], v[34:35], v[2:3] op_sel_hi:[1,0]
	v_pk_mul_f32 v[32:33], v[32:33], v[2:3] op_sel_hi:[1,0]
	v_pk_mul_f32 v[30:31], v[30:31], v[2:3] op_sel_hi:[1,0]
	v_pk_mul_f32 v[28:29], v[28:29], v[2:3] op_sel_hi:[1,0]
	v_pk_mul_f32 v[26:27], v[26:27], v[2:3] op_sel_hi:[1,0]
	v_pk_mul_f32 v[24:25], v[24:25], v[2:3] op_sel_hi:[1,0]
	v_pk_mul_f32 v[22:23], v[22:23], v[2:3] op_sel_hi:[1,0]
	v_pk_mul_f32 v[20:21], v[20:21], v[2:3] op_sel_hi:[1,0]
	v_pk_mul_f32 v[18:19], v[18:19], v[2:3] op_sel_hi:[1,0]
